# baseline (speedup 1.0000x reference)
_Z11attn_kernelPKDF16_S0_S0_PKjPf:
	s_and_b32 s27, s2, 7
	s_lshr_b32 s3, s2, 3
	s_lshr_b32 s12, s2, 6
	v_readfirstlane_b32 s23, v0
	s_mov_b32 s13, 0
	s_lshl_b32 s2, s2, 5
	s_load_dwordx8 s[4:11], s[0:1], 0x0
	s_and_b32 s28, s3, 0x1ffffff8
	s_lshr_b32 s20, s23, 6
	s_lshl_b64 s[14:15], s[12:13], 11
	s_and_b32 s2, s2, 0x700
	s_or_b32 s16, s28, s27
	s_or_b32 s2, s14, s2
	s_lshl_b32 s3, s20, 5
	s_add_u32 s2, s2, s3
	s_addc_u32 s3, s15, 0
	s_lshl_b64 s[14:15], s[2:3], 10
	s_waitcnt lgkmcnt(0)
	s_add_u32 s4, s4, s14
	s_addc_u32 s5, s5, s15
	s_lshl_b32 s12, s27, 7
	s_add_u32 s4, s4, s12
	s_mov_b32 s17, s13
	s_addc_u32 s5, s5, 0
	s_lshl_b64 s[12:13], s[16:17], 18
	s_add_u32 s14, s6, s12
	s_addc_u32 s15, s7, s13
	s_add_u32 s12, s8, s12
	s_addc_u32 s13, s9, s13
	s_lshl_b32 s22, s20, 10
	s_cmp_lg_u32 0, -1
	v_and_b32_e32 v1, 63, v0
	s_cselect_b32 s6, 0, 0
	v_lshl_or_b32 v189, v1, 4, s22
	s_add_i32 s24, s22, s6
	s_mov_b32 s6, m0
	s_mov_b32 m0, s24
	s_nop 0
	global_load_lds_dwordx4 v189, s[14:15] sc1
	s_mov_b32 m0, s6
	v_bfe_u32 v18, v0, 5, 1
	s_add_i32 s25, s24, 0x6000
	s_mov_b32 s6, m0
	s_mov_b32 m0, s25
	s_nop 0
	global_load_lds_dwordx4 v189, s[12:13] sc1
	s_mov_b32 m0, s6
	v_and_b32_e32 v181, 31, v0
	s_add_u32 s6, s14, 0x2000
	v_lshlrev_b32_e32 v184, 4, v18
	s_addc_u32 s7, s15, 0
	s_add_i32 s17, s24, 0x2000
	s_mov_b32 s18, m0
	s_mov_b32 m0, s17
	s_nop 0
	global_load_lds_dwordx4 v189, s[6:7] sc1
	s_mov_b32 m0, s18
	v_lshl_or_b32 v2, v181, 10, v184
	global_load_dwordx4 v[124:127], v2, s[4:5]
	global_load_dwordx4 v[120:123], v2, s[4:5] offset:32
	global_load_dwordx4 v[116:119], v2, s[4:5] offset:64
	global_load_dwordx4 v[112:115], v2, s[4:5] offset:96
	v_lshlrev_b32_e32 v182, 10, v18
	v_lshlrev_b32_e32 v19, 4, v181
	v_add3_u32 v190, 0, v182, v19
	s_lshl_b32 s5, s16, 2
	s_load_dword s5, s[10:11], s5 offset:0x0
	s_mov_b32 s4, 0x42a20000
	v_mov_b32_e32 v2, 0
	v_mov_b32_e32 v3, v2
	v_mov_b32_e32 v4, v2
	v_mov_b32_e32 v5, v2
	v_mov_b32_e32 v6, v2
	v_mov_b32_e32 v7, v2
	v_mov_b32_e32 v8, v2
	v_mov_b32_e32 v9, v2
	v_mov_b32_e32 v10, v2
	v_mov_b32_e32 v11, v2
	v_mov_b32_e32 v12, v2
	v_mov_b32_e32 v13, v2
	v_mov_b32_e32 v14, v2
	v_mov_b32_e32 v15, v2
	v_mov_b32_e32 v16, v2
	v_mov_b32_e32 v17, v2
	s_waitcnt vmcnt(3)
	v_fma_mix_f32 v19, v124, v124, 0 op_sel_hi:[1,1,0]
	s_nop 0
	v_fma_mix_f32 v19, v124, v124, v19 op_sel:[1,1,0] op_sel_hi:[1,1,0]
	s_nop 0
	v_fma_mix_f32 v19, v125, v125, v19 op_sel_hi:[1,1,0]
	s_nop 0
	v_fma_mix_f32 v19, v125, v125, v19 op_sel:[1,1,0] op_sel_hi:[1,1,0]
	s_nop 0
	v_fma_mix_f32 v19, v126, v126, v19 op_sel_hi:[1,1,0]
	s_nop 0
	v_fma_mix_f32 v19, v126, v126, v19 op_sel:[1,1,0] op_sel_hi:[1,1,0]
	s_nop 0
	v_fma_mix_f32 v19, v127, v127, v19 op_sel_hi:[1,1,0]
	s_nop 0
	v_fma_mix_f32 v19, v127, v127, v19 op_sel:[1,1,0] op_sel_hi:[1,1,0]
	s_waitcnt vmcnt(2)
	v_fma_mix_f32 v19, v120, v120, v19 op_sel_hi:[1,1,0]
	s_nop 0
	v_fma_mix_f32 v19, v120, v120, v19 op_sel:[1,1,0] op_sel_hi:[1,1,0]
	s_nop 0
	v_fma_mix_f32 v19, v121, v121, v19 op_sel_hi:[1,1,0]
	s_nop 0
	v_fma_mix_f32 v19, v121, v121, v19 op_sel:[1,1,0] op_sel_hi:[1,1,0]
	s_nop 0
	v_fma_mix_f32 v19, v122, v122, v19 op_sel_hi:[1,1,0]
	s_nop 0
	v_fma_mix_f32 v19, v122, v122, v19 op_sel:[1,1,0] op_sel_hi:[1,1,0]
	s_nop 0
	v_fma_mix_f32 v19, v123, v123, v19 op_sel_hi:[1,1,0]
	s_nop 0
	v_fma_mix_f32 v19, v123, v123, v19 op_sel:[1,1,0] op_sel_hi:[1,1,0]
	s_waitcnt vmcnt(1)
	v_fma_mix_f32 v19, v116, v116, v19 op_sel_hi:[1,1,0]
	s_nop 0
	v_fma_mix_f32 v19, v116, v116, v19 op_sel:[1,1,0] op_sel_hi:[1,1,0]
	s_nop 0
	v_fma_mix_f32 v19, v117, v117, v19 op_sel_hi:[1,1,0]
	s_nop 0
	v_fma_mix_f32 v19, v117, v117, v19 op_sel:[1,1,0] op_sel_hi:[1,1,0]
	s_nop 0
	v_fma_mix_f32 v19, v118, v118, v19 op_sel_hi:[1,1,0]
	s_nop 0
	v_fma_mix_f32 v19, v118, v118, v19 op_sel:[1,1,0] op_sel_hi:[1,1,0]
	s_nop 0
	v_fma_mix_f32 v19, v119, v119, v19 op_sel_hi:[1,1,0]
	s_nop 0
	v_fma_mix_f32 v19, v119, v119, v19 op_sel:[1,1,0] op_sel_hi:[1,1,0]
	s_waitcnt vmcnt(0)
	v_fma_mix_f32 v19, v112, v112, v19 op_sel_hi:[1,1,0]
	s_nop 0
	v_fma_mix_f32 v19, v112, v112, v19 op_sel:[1,1,0] op_sel_hi:[1,1,0]
	s_nop 0
	v_fma_mix_f32 v19, v113, v113, v19 op_sel_hi:[1,1,0]
	s_nop 0
	v_fma_mix_f32 v19, v113, v113, v19 op_sel:[1,1,0] op_sel_hi:[1,1,0]
	s_nop 0
	v_fma_mix_f32 v19, v114, v114, v19 op_sel_hi:[1,1,0]
	s_nop 0
	v_fma_mix_f32 v19, v114, v114, v19 op_sel:[1,1,0] op_sel_hi:[1,1,0]
	s_nop 0
	v_fma_mix_f32 v19, v115, v115, v19 op_sel_hi:[1,1,0]
	s_nop 0
	v_fma_mix_f32 v19, v115, v115, v19 op_sel:[1,1,0] op_sel_hi:[1,1,0]
	s_nop 0
	v_mov_b32_e32 v20, v19
	s_nop 1
	v_permlane32_swap_b32_e32 v19, v20
	v_add_f32_e32 v19, v19, v20
	s_waitcnt lgkmcnt(0)
	v_mul_f32_e32 v19, s5, v19
	v_cmp_ge_f32_e32 vcc, s4, v19
	s_cmp_eq_u64 vcc, exec
	s_cselect_b64 s[4:5], -1, 0
	s_add_u32 s6, s14, 0x4000
	s_addc_u32 s7, s15, 0
	s_add_i32 s10, s24, 0x4000
	s_mov_b32 s11, m0
	s_mov_b32 m0, s10
	s_nop 0
	global_load_lds_dwordx4 v189, s[6:7] sc1
	s_mov_b32 m0, s11
	s_waitcnt vmcnt(3) lgkmcnt(0)
	s_barrier
	ds_read_b128 v[20:23], v190
	ds_read_b128 v[24:27], v190 offset:512
	s_waitcnt lgkmcnt(1)
	v_mfma_f32_32x32x16_f16 v[96:111], v[20:23], v[124:127], v[2:17]
	v_cndmask_b32_e64 v19, 0, 1, s[4:5]
	s_nop 0
	v_readfirstlane_b32 s4, v19
	s_bitcmp1_b32 s4, 0
	s_cselect_b64 s[16:17], -1, 0
	s_xor_b64 s[18:19], s[16:17], -1
	s_mov_b64 s[4:5], -1
	s_waitcnt lgkmcnt(0)
	v_mfma_f32_32x32x16_f16 v[80:95], v[24:27], v[124:127], v[2:17]
	ds_read_b128 v[20:23], v190 offset:2048
	ds_read_b128 v[24:27], v190 offset:2560
	s_and_b64 vcc, exec, s[18:19]
	s_waitcnt lgkmcnt(1)
	v_mfma_f32_32x32x16_f16 v[96:111], v[20:23], v[120:123], v[96:111]
	s_waitcnt lgkmcnt(0)
	v_mfma_f32_32x32x16_f16 v[80:95], v[24:27], v[120:123], v[80:95]
	ds_read_b128 v[20:23], v190 offset:4096
	ds_read_b128 v[24:27], v190 offset:4608
	s_waitcnt lgkmcnt(1)
	v_mfma_f32_32x32x16_f16 v[96:111], v[20:23], v[116:119], v[96:111]
	s_waitcnt lgkmcnt(0)
	v_mfma_f32_32x32x16_f16 v[80:95], v[24:27], v[116:119], v[80:95]
	ds_read_b128 v[20:23], v190 offset:6144
	ds_read_b128 v[24:27], v190 offset:6656
	s_waitcnt lgkmcnt(1)
	v_mfma_f32_32x32x16_f16 v[96:111], v[20:23], v[112:115], v[96:111]
	s_waitcnt lgkmcnt(0)
	v_mfma_f32_32x32x16_f16 v[80:95], v[24:27], v[112:115], v[80:95]
	s_cbranch_vccz .LBB2_2
	v_max3_f32 v19, v96, v97, v80
	v_max3_f32 v20, v98, v99, v81
	s_nop 0
	v_max3_f32 v19, v19, v82, v83
	v_max3_f32 v20, v20, v102, v103
	s_nop 0
	v_max3_f32 v19, v19, v100, v101
	v_max3_f32 v20, v20, v86, v87
	s_nop 0
	v_max3_f32 v19, v19, v84, v85
	v_max3_f32 v20, v20, v106, v107
	s_nop 0
	v_max3_f32 v19, v19, v104, v105
	v_max3_f32 v20, v20, v90, v91
	s_nop 0
	v_max3_f32 v19, v19, v88, v89
	v_max3_f32 v20, v20, v110, v111
	s_nop 0
	v_max3_f32 v19, v19, v108, v109
	v_max3_f32 v20, v20, v94, v95
	s_nop 0
	v_max3_f32 v19, v19, v92, v93
	s_nop 0
	v_max_f32 v19, v19, v20
	s_nop 0
	v_mov_b32_e32 v20, v19
	s_nop 1
	v_permlane32_swap_b32_e32 v19, v20
	v_max_f32 v180, v19, v20
	s_nop 0
	v_sub_f32_e32 v19, v96, v180
	v_exp_f32_e32 v64, v19
	v_sub_f32_e32 v19, v80, v180
	v_exp_f32_e32 v48, v19
	v_sub_f32_e32 v19, v97, v180
	v_exp_f32_e32 v65, v19
	v_sub_f32_e32 v19, v81, v180
	v_exp_f32_e32 v49, v19
	v_sub_f32_e32 v19, v98, v180
	v_exp_f32_e32 v66, v19
	v_sub_f32_e32 v19, v82, v180
	v_exp_f32_e32 v50, v19
	v_sub_f32_e32 v19, v99, v180
	v_exp_f32_e32 v67, v19
	v_sub_f32_e32 v19, v83, v180
	v_exp_f32_e32 v51, v19
	v_sub_f32_e32 v19, v100, v180
	v_exp_f32_e32 v68, v19
	v_sub_f32_e32 v19, v84, v180
	v_exp_f32_e32 v52, v19
	v_sub_f32_e32 v19, v101, v180
	v_exp_f32_e32 v69, v19
	v_sub_f32_e32 v19, v85, v180
	v_exp_f32_e32 v53, v19
	v_sub_f32_e32 v19, v102, v180
	v_exp_f32_e32 v70, v19
	v_sub_f32_e32 v19, v86, v180
	v_exp_f32_e32 v54, v19
	v_sub_f32_e32 v19, v103, v180
	v_exp_f32_e32 v71, v19
	v_sub_f32_e32 v19, v87, v180
	v_exp_f32_e32 v55, v19
	v_sub_f32_e32 v19, v104, v180
	v_exp_f32_e32 v72, v19
	v_sub_f32_e32 v19, v105, v180
	v_exp_f32_e32 v73, v19
	v_sub_f32_e32 v19, v106, v180
	v_exp_f32_e32 v74, v19
	v_sub_f32_e32 v19, v107, v180
	v_exp_f32_e32 v75, v19
	v_sub_f32_e32 v19, v108, v180
	v_exp_f32_e32 v76, v19
	v_sub_f32_e32 v19, v109, v180
	v_exp_f32_e32 v77, v19
	v_sub_f32_e32 v19, v110, v180
	v_xor_b32_e32 v32, 0x80000000, v180
	v_exp_f32_e32 v78, v19
	v_sub_f32_e32 v19, v111, v180
	v_mov_b32_e32 v33, v32
	v_mov_b32_e32 v34, v32
	v_mov_b32_e32 v35, v32
	v_mov_b32_e32 v36, v32
	v_mov_b32_e32 v37, v32
	v_mov_b32_e32 v38, v32
	v_mov_b32_e32 v39, v32
	v_mov_b32_e32 v40, v32
	v_mov_b32_e32 v41, v32
	v_mov_b32_e32 v42, v32
	v_mov_b32_e32 v43, v32
	v_mov_b32_e32 v44, v32
	v_mov_b32_e32 v45, v32
	v_mov_b32_e32 v46, v32
	v_mov_b32_e32 v47, v32
	v_pk_add_f32 v[56:57], v[88:89], v[180:181] op_sel_hi:[1,0] neg_lo:[0,1] neg_hi:[0,1]
	v_pk_add_f32 v[58:59], v[90:91], v[180:181] op_sel_hi:[1,0] neg_lo:[0,1] neg_hi:[0,1]
	v_pk_add_f32 v[60:61], v[92:93], v[180:181] op_sel_hi:[1,0] neg_lo:[0,1] neg_hi:[0,1]
	v_exp_f32_e32 v79, v19
	v_pk_add_f32 v[62:63], v[94:95], v[180:181] op_sel_hi:[1,0] neg_lo:[0,1] neg_hi:[0,1]
	s_load_dwordx2 s[6:7], s[0:1], 0x20
	s_lshl_b32 s21, s27, 6
	s_cbranch_execz .LBB2_3
	s_branch .LBB2_4

.LBB2_4:
	s_and_b32 s0, s23, 0x3fffffc0
	s_lshl_b32 s0, s0, 2
	s_lshl_b64 s[10:11], s[2:3], 9
	s_add_i32 s23, s0, 0
	s_add_u32 s0, s14, 0x6000
	s_waitcnt vmcnt(0) lgkmcnt(0)
	s_barrier
	s_addc_u32 s1, s15, 0
	s_mov_b32 s2, m0
	s_mov_b32 m0, s24
	s_nop 0
	global_load_lds_dwordx4 v189, s[0:1] sc1
	s_mov_b32 m0, s2
	s_add_u32 s0, s12, 0x2000
	s_addc_u32 s1, s13, 0
	s_cmp_lg_u32 0, -1
	s_cselect_b32 s2, 0, 0
	s_add_i32 s2, s2, s22
	s_add_i32 s2, s2, 0x8000
	s_mov_b32 s4, m0
	s_mov_b32 m0, s2
	s_nop 0
	global_load_lds_dwordx4 v189, s[0:1] sc1
	s_mov_b32 m0, s4
	ds_read_b128 v[172:175], v190 offset:8192
	ds_read_b128 v[168:171], v190 offset:8704
	ds_read_b128 v[164:167], v190 offset:10240
	ds_read_b128 v[160:163], v190 offset:10752
	ds_read_b128 v[156:159], v190 offset:12288
	ds_read_b128 v[152:155], v190 offset:12800
	ds_read_b128 v[148:151], v190 offset:14336
	ds_read_b128 v[144:147], v190 offset:14848
	s_mov_b32 s3, 0
	s_add_i32 s2, s28, s27
	s_lshl_b64 s[4:5], s[2:3], 18
	v_lshlrev_b32_e32 v2, 1, v1
	v_lshlrev_b32_e32 v3, 3, v0
	s_add_u32 s2, s8, s4
	v_and_b32_e32 v2, 32, v2
	v_and_b32_e32 v3, 24, v3
	v_lshlrev_b32_e32 v185, 4, v0
	s_waitcnt vmcnt(2) lgkmcnt(0)
	s_barrier
	s_addc_u32 s4, s9, s5
	v_add3_u32 v2, 0, v2, v3
	v_lshlrev_b32_e32 v3, 8, v18
	v_and_b32_e32 v0, 0xc0, v185
	s_add_u32 s27, s2, 0x2000
	v_mov_b32_e32 v188, 0
	v_lshrrev_b32_e32 v183, 4, v1
	v_add3_u32 v187, v2, v3, v0
	s_mov_b32 s26, -1
	v_cmp_gt_u32_e64 s[0:1], 32, v1
	v_lshl_add_u32 v186, v181, 2, s23
	s_addc_u32 s28, s4, 0
	s_movk_i32 s29, 0x4000
	s_movk_i32 s31, 0x2000
	s_mov_b64 s[8:9], 0
	s_mov_b32 s30, 0x41000000
	v_mov_b32_e32 v0, 0
	v_mov_b32_e32 v1, v188
	v_mov_b32_e32 v2, v188
	v_mov_b32_e32 v3, v188
	v_mov_b32_e32 v4, v188
	v_mov_b32_e32 v5, v188
	v_mov_b32_e32 v6, v188
	v_mov_b32_e32 v7, v188
	v_mov_b32_e32 v8, v188
	v_mov_b32_e32 v9, v188
	v_mov_b32_e32 v10, v188
	v_mov_b32_e32 v11, v188
	v_mov_b32_e32 v12, v188
	v_mov_b32_e32 v13, v188
	v_mov_b32_e32 v14, v188
	v_mov_b32_e32 v15, v188
	v_mov_b32_e32 v16, 0
	v_mov_b32_e32 v17, v188
	v_mov_b32_e32 v18, v188
	v_mov_b32_e32 v19, v188
	v_mov_b32_e32 v20, v188
	v_mov_b32_e32 v21, v188
	v_mov_b32_e32 v22, v188
	v_mov_b32_e32 v23, v188
	v_mov_b32_e32 v24, v188
	v_mov_b32_e32 v25, v188
	v_mov_b32_e32 v26, v188
	v_mov_b32_e32 v27, v188
	v_mov_b32_e32 v28, v188
	v_mov_b32_e32 v29, v188
	v_mov_b32_e32 v30, v188
	v_mov_b32_e32 v31, v188
	s_cmp_ge_u32 s20, 4
	s_cbranch_scc0 .Lattn_prio_done
	s_setprio 1
.Lattn_prio_done:
.LBB2_5:
	s_add_i32 s26, s26, 2
	v_add_u32_e32 v191, s3, v187
	ds_read_b64_tr_b16 v[176:177], v191 offset:24576
	ds_read_b64_tr_b16 v[178:179], v191 offset:25088
	s_waitcnt lgkmcnt(0)
	v_mfma_f32_32x32x16_f16 v[96:111], v[172:175], v[124:127], v[32:47]
	v_exp_f32_e32 v56, v56
	v_exp_f32_e32 v57, v57
	v_cvt_pk_f16_f32 v140, v64, v65
	v_cvt_pk_f16_f32 v141, v66, v67
	ds_read_b64_tr_b16 v[172:173], v191 offset:28672
	ds_read_b64_tr_b16 v[174:175], v191 offset:29184
	v_mfma_f32_32x32x16_f16 v[80:95], v[168:171], v[124:127], v[32:47]
	v_exp_f32_e32 v58, v58
	v_exp_f32_e32 v59, v59
	v_pk_add_f16 v128, v140, v141
	v_cvt_pk_f16_f32 v142, v68, v69
	v_cvt_pk_f16_f32 v143, v70, v71
	ds_read_b64_tr_b16 v[64:65], v191 offset:25600
	ds_read_b64_tr_b16 v[66:67], v191 offset:26112
	v_mfma_f32_32x32x16_f16 v[96:111], v[164:167], v[120:123], v[96:111]
	v_exp_f32_e32 v60, v60
	v_exp_f32_e32 v61, v61
	v_pk_add_f16 v129, v142, v143
	v_cvt_pk_f16_f32 v136, v72, v73
	v_cvt_pk_f16_f32 v137, v74, v75
	ds_read_b64_tr_b16 v[68:69], v191 offset:29696
	ds_read_b64_tr_b16 v[70:71], v191 offset:30208
	v_mfma_f32_32x32x16_f16 v[80:95], v[160:163], v[120:123], v[80:95]
	v_exp_f32_e32 v62, v62
	v_exp_f32_e32 v63, v63
	v_pk_add_f16 v72, v136, v137
	v_pk_add_f16 v128, v128, v129
	v_cvt_pk_f16_f32 v138, v76, v77
	v_cvt_pk_f16_f32 v139, v78, v79
	s_min_u32 s2, s26, 28
	s_lshl_b32 s2, s2, 13
	s_add_u32 s2, s14, s2
	s_addc_u32 s3, s15, 0
	s_add_u32 s2, s2, 0x6000
	s_addc_u32 s3, s3, 0
	s_add_i32 s4, s31, s24
	s_mov_b32 s5, m0
	s_mov_b32 m0, s4
	s_nop 0
	global_load_lds_dwordx4 v189, s[2:3] sc1
	s_mov_b32 m0, s5
	ds_read_b64_tr_b16 v[76:77], v191 offset:26624
	ds_read_b64_tr_b16 v[78:79], v191 offset:27136
	v_mfma_f32_32x32x16_f16 v[96:111], v[156:159], v[116:119], v[96:111]
	v_pk_add_f16 v73, v138, v139
	v_cvt_pk_f16_f32 v132, v48, v49
	v_cvt_pk_f16_f32 v133, v50, v51
	ds_read_b64_tr_b16 v[48:49], v191 offset:30720
	ds_read_b64_tr_b16 v[50:51], v191 offset:31232
	v_mfma_f32_32x32x16_f16 v[80:95], v[152:155], v[116:119], v[80:95]
	v_pk_add_f16 v129, v72, v73
	v_cvt_pk_f16_f32 v134, v52, v53
	v_cvt_pk_f16_f32 v135, v54, v55
	v_pk_add_f16 v156, v132, v133
	s_add_u32 s2, s27, 0x2000
	s_addc_u32 s3, s28, 0
	s_add_i32 s4, s29, s25
	s_mov_b32 s5, m0
	s_mov_b32 m0, s4
	s_nop 0
	global_load_lds_dwordx4 v189, s[2:3] sc1
	s_mov_b32 m0, s5
	ds_read_b64_tr_b16 v[72:73], v191 offset:27648
	ds_read_b64_tr_b16 v[74:75], v191 offset:28160
	v_mfma_f32_32x32x16_f16 v[96:111], v[148:151], v[112:115], v[96:111]
	v_pk_add_f16 v153, v128, v129
	v_cvt_pk_f16_f32 v128, v56, v57
	v_cvt_pk_f16_f32 v129, v58, v59
	v_pk_add_f16 v152, v134, v135
	ds_read_b64_tr_b16 v[52:53], v191 offset:31744
	ds_read_b64_tr_b16 v[54:55], v191 offset:32256
	v_mfma_f32_32x32x16_f16 v[80:95], v[144:147], v[112:115], v[80:95]
	v_pk_add_f16 v56, v128, v129
	v_pk_add_f16 v57, v156, v152
	v_cvt_pk_f16_f32 v130, v60, v61
	v_cvt_pk_f16_f32 v131, v62, v63
	v_cndmask_b32_e64 v58, 0, 1, s[18:19]
	v_cmp_ne_u32_e64 s[2:3], 1, v58
	s_andn2_b64 vcc, exec, s[18:19]
	v_pk_add_f16 v57, v153, v57
	v_pk_add_f16 v58, v130, v131
	s_cbranch_vccnz .LBB2_7
	v_pk_add_f16 v59, v56, v58
	v_max3_f32 v61, v96, v97, v80
	v_max3_f32 v62, v98, v99, v81
	s_mov_b64 s[8:9], 0
	v_pk_add_f16 v59, v57, v59
	s_nop 0
	v_cvt_f32_f16_e32 v60, v59
	v_cvt_f32_f16_sdwa v59, v59 dst_sel:DWORD dst_unused:UNUSED_PAD src0_sel:WORD_1
	v_add_f32_e32 v59, v59, v60
	v_add_f32_e32 v188, v188, v59
	v_max3_f32 v59, v61, v82, v83
	v_max3_f32 v60, v62, v102, v103
	s_nop 0
	v_max3_f32 v59, v59, v100, v101
	v_max3_f32 v60, v60, v86, v87
	s_nop 0
	v_max3_f32 v59, v59, v84, v85
	v_max3_f32 v60, v60, v106, v107
	s_nop 0
	v_max3_f32 v59, v59, v104, v105
	v_max3_f32 v60, v60, v90, v91
	s_nop 0
	v_max3_f32 v59, v59, v88, v89
	v_max3_f32 v60, v60, v110, v111
	s_nop 0
	v_max3_f32 v59, v59, v108, v109
	v_max3_f32 v60, v60, v94, v95
	s_nop 0
	v_max3_f32 v59, v59, v92, v93
	s_nop 0
	v_max_f32 v59, v59, v60
	s_nop 0
	v_mov_b32_e32 v60, v59
	s_nop 1
	v_permlane32_swap_b32_e32 v59, v60
	v_max_f32 v59, v59, v60
	s_nop 0
	v_cmp_lt_f32_e32 vcc, s30, v59
	s_cbranch_vccnz .LBB2_19

.LBB2_11:
	s_add_i32 s33, s29, 0x2000
	s_cmpk_lg_i32 s29, 0x4000
	s_cselect_b32 s33, s33, 0
	v_add_u32_e32 v191, s31, v187
	ds_read_b64_tr_b16 v[148:149], v191 offset:24576
	ds_read_b64_tr_b16 v[150:151], v191 offset:25088
	s_waitcnt lgkmcnt(9)
	v_mfma_f32_32x32x16_f16 v[64:79], v[56:59], v[124:127], v[32:47]
	v_exp_f32_e32 v88, v88
	v_exp_f32_e32 v89, v89
	v_cvt_pk_f16_f32 v140, v96, v97
	v_cvt_pk_f16_f32 v141, v98, v99
	ds_read_b64_tr_b16 v[144:145], v191 offset:28672
	ds_read_b64_tr_b16 v[146:147], v191 offset:29184
	s_waitcnt lgkmcnt(10)
	v_mfma_f32_32x32x16_f16 v[48:63], v[176:179], v[124:127], v[32:47]
	v_exp_f32_e32 v90, v90
	v_exp_f32_e32 v91, v91
	v_pk_add_f16 v128, v140, v141
	v_cvt_pk_f16_f32 v142, v100, v101
	v_cvt_pk_f16_f32 v143, v102, v103
	ds_read_b64_tr_b16 v[96:97], v191 offset:25600
	ds_read_b64_tr_b16 v[98:99], v191 offset:26112
	s_waitcnt lgkmcnt(11)
	v_mfma_f32_32x32x16_f16 v[64:79], v[172:175], v[120:123], v[64:79]
	v_exp_f32_e32 v92, v92
	v_exp_f32_e32 v93, v93
	v_pk_add_f16 v129, v142, v143
	v_cvt_pk_f16_f32 v136, v104, v105
	v_cvt_pk_f16_f32 v137, v106, v107
	ds_read_b64_tr_b16 v[100:101], v191 offset:29696
	ds_read_b64_tr_b16 v[102:103], v191 offset:30208
	s_waitcnt lgkmcnt(12)
	v_mfma_f32_32x32x16_f16 v[48:63], v[168:171], v[120:123], v[48:63]
	v_exp_f32_e32 v94, v94
	v_exp_f32_e32 v95, v95
	v_pk_add_f16 v128, v128, v129
	v_cvt_pk_f16_f32 v138, v108, v109
	v_cvt_pk_f16_f32 v139, v110, v111
	v_pk_add_f16 v172, v136, v137
	s_min_u32 s31, s26, 27
	s_lshl_b32 s31, s31, 13
	s_add_u32 s31, s14, s31
	s_addc_u32 s35, s15, 0
	s_add_u32 s34, s31, 0x8000
	s_addc_u32 s35, s35, 0
	s_add_i32 s31, s29, s24
	s_mov_b32 s36, m0
	s_mov_b32 m0, s31
	s_nop 0
	global_load_lds_dwordx4 v189, s[34:35] sc1
	s_mov_b32 m0, s36
	ds_read_b64_tr_b16 v[104:105], v191 offset:26624
	ds_read_b64_tr_b16 v[106:107], v191 offset:27136
	s_waitcnt lgkmcnt(13)
	v_mfma_f32_32x32x16_f16 v[64:79], v[164:167], v[116:119], v[64:79]
	v_pk_add_f16 v108, v138, v139
	v_cvt_pk_f16_f32 v132, v80, v81
	v_cvt_pk_f16_f32 v133, v82, v83
	ds_read_b64_tr_b16 v[80:81], v191 offset:30720
	ds_read_b64_tr_b16 v[82:83], v191 offset:31232
	s_waitcnt lgkmcnt(14)
	v_mfma_f32_32x32x16_f16 v[48:63], v[160:163], v[116:119], v[48:63]
	v_pk_add_f16 v129, v172, v108
	v_cvt_pk_f16_f32 v134, v84, v85
	v_cvt_pk_f16_f32 v135, v86, v87
	v_pk_add_f16 v164, v132, v133
	s_add_u32 s34, s27, 0x4000
	s_addc_u32 s35, s28, 0
	s_add_i32 s31, s33, s25
	s_mov_b32 s36, m0
	s_mov_b32 m0, s31
	s_nop 0
	global_load_lds_dwordx4 v189, s[34:35] sc1
	s_mov_b32 m0, s36
	ds_read_b64_tr_b16 v[108:109], v191 offset:27648
	ds_read_b64_tr_b16 v[110:111], v191 offset:28160
	s_waitcnt lgkmcnt(14)
	v_mfma_f32_32x32x16_f16 v[64:79], v[156:159], v[112:115], v[64:79]
	v_pk_add_f16 v161, v128, v129
	v_cvt_pk_f16_f32 v128, v88, v89
	v_cvt_pk_f16_f32 v129, v90, v91
	v_pk_add_f16 v160, v134, v135
	ds_read_b64_tr_b16 v[84:85], v191 offset:31744
	ds_read_b64_tr_b16 v[86:87], v191 offset:32256
	v_mfma_f32_32x32x16_f16 v[48:63], v[152:155], v[112:115], v[48:63]
	v_pk_add_f16 v88, v128, v129
	v_pk_add_f16 v89, v164, v160
	v_cvt_pk_f16_f32 v130, v92, v93
	v_cvt_pk_f16_f32 v131, v94, v95
	s_and_b64 vcc, exec, s[2:3]
	v_pk_add_f16 v89, v161, v89
	v_pk_add_f16 v90, v130, v131
	s_cbranch_vccnz .LBB2_13
	v_pk_add_f16 v91, v88, v90
	v_max3_f32 v93, v64, v65, v48
	v_max3_f32 v94, v66, v67, v49
	s_mov_b64 s[8:9], 0
	v_pk_add_f16 v91, v89, v91
	s_nop 0
	v_cvt_f32_f16_e32 v92, v91
	v_cvt_f32_f16_sdwa v91, v91 dst_sel:DWORD dst_unused:UNUSED_PAD src0_sel:WORD_1
	v_add_f32_e32 v91, v91, v92
	v_add_f32_e32 v188, v188, v91
	v_max3_f32 v91, v93, v50, v51
	v_max3_f32 v92, v94, v70, v71
	s_nop 0
	v_max3_f32 v91, v91, v68, v69
	v_max3_f32 v92, v92, v54, v55
	s_nop 0
	v_max3_f32 v91, v91, v52, v53
	v_max3_f32 v92, v92, v74, v75
	s_nop 0
	v_max3_f32 v91, v91, v72, v73
	v_max3_f32 v92, v92, v58, v59
	s_nop 0
	v_max3_f32 v91, v91, v56, v57
	v_max3_f32 v92, v92, v78, v79
	s_nop 0
	v_max3_f32 v91, v91, v76, v77
	v_max3_f32 v92, v92, v62, v63
	s_nop 0
	v_max3_f32 v91, v91, v60, v61
	s_nop 0
	v_max_f32 v91, v91, v92
	s_nop 0
	v_mov_b32_e32 v92, v91
	s_nop 1
	v_permlane32_swap_b32_e32 v91, v92
	v_max_f32 v91, v91, v92
	s_nop 0
	v_cmp_lt_f32_e32 vcc, s30, v91
	s_cbranch_vccnz .LBB2_22

.LBB2_25:
	ds_read_b64_tr_b16 v[96:97], v187 offset:24576
	ds_read_b64_tr_b16 v[98:99], v187 offset:25088
	s_waitcnt lgkmcnt(9)
	v_mfma_f32_32x32x16_f16 v[80:95], v[172:175], v[124:127], v[32:47]
	v_exp_f32_e32 v56, v56
	v_exp_f32_e32 v57, v57
	v_cvt_pk_f16_f32 v140, v64, v65
	v_cvt_pk_f16_f32 v141, v66, v67
	ds_read_b64_tr_b16 v[64:65], v187 offset:28672
	ds_read_b64_tr_b16 v[66:67], v187 offset:29184
	s_waitcnt lgkmcnt(10)
	v_mfma_f32_32x32x16_f16 v[32:47], v[168:171], v[124:127], v[32:47]
	v_exp_f32_e32 v58, v58
	v_exp_f32_e32 v59, v59
	v_pk_add_f16 v100, v140, v141
	v_cvt_pk_f16_f32 v142, v68, v69
	v_cvt_pk_f16_f32 v143, v70, v71
	ds_read_b64_tr_b16 v[68:69], v187 offset:25600
	ds_read_b64_tr_b16 v[70:71], v187 offset:26112
	s_waitcnt lgkmcnt(11)
	v_mfma_f32_32x32x16_f16 v[80:95], v[164:167], v[120:123], v[80:95]
	v_exp_f32_e32 v60, v60
	v_exp_f32_e32 v61, v61
	v_pk_add_f16 v101, v142, v143
	v_cvt_pk_f16_f32 v136, v72, v73
	v_cvt_pk_f16_f32 v137, v74, v75
	ds_read_b64_tr_b16 v[72:73], v187 offset:29696
	ds_read_b64_tr_b16 v[74:75], v187 offset:30208
	s_waitcnt lgkmcnt(12)
	v_mfma_f32_32x32x16_f16 v[32:47], v[160:163], v[120:123], v[32:47]
	v_exp_f32_e32 v62, v62
	v_exp_f32_e32 v63, v63
	v_pk_add_f16 v102, v136, v137
	v_pk_add_f16 v100, v100, v101
	v_cvt_pk_f16_f32 v138, v76, v77
	v_cvt_pk_f16_f32 v139, v78, v79
	s_add_u32 s14, s14, 0x3e000
	s_addc_u32 s15, s15, 0
	s_cmp_lg_u32 0, -1
	s_cselect_b32 s16, 0, 0
	s_add_i32 s16, s16, s22
	s_add_i32 s17, s16, 0x2000
	s_mov_b32 s18, m0
	s_mov_b32 m0, s17
	s_nop 0
	global_load_lds_dwordx4 v189, s[14:15] sc1
	s_mov_b32 m0, s18
	ds_read_b64_tr_b16 v[104:105], v187 offset:26624
	ds_read_b64_tr_b16 v[106:107], v187 offset:27136
	s_waitcnt lgkmcnt(13)
	v_mfma_f32_32x32x16_f16 v[80:95], v[156:159], v[116:119], v[80:95]
	v_pk_add_f16 v101, v138, v139
	v_cvt_pk_f16_f32 v132, v48, v49
	v_cvt_pk_f16_f32 v133, v50, v51
	ds_read_b64_tr_b16 v[76:77], v187 offset:30720
	ds_read_b64_tr_b16 v[78:79], v187 offset:31232
	s_waitcnt lgkmcnt(14)
	v_mfma_f32_32x32x16_f16 v[32:47], v[152:155], v[116:119], v[32:47]
	v_pk_add_f16 v49, v102, v101
	v_cvt_pk_f16_f32 v134, v52, v53
	v_cvt_pk_f16_f32 v135, v54, v55
	v_pk_add_f16 v48, v132, v133
	s_add_u32 s12, s12, 0x3e000
	s_addc_u32 s13, s13, 0
	s_add_i32 s16, s16, 0xa000
	s_mov_b32 s14, m0
	s_mov_b32 m0, s16
	s_nop 0
	global_load_lds_dwordx4 v189, s[12:13] sc1
	s_mov_b32 m0, s14
	ds_read_b64_tr_b16 v[108:109], v187 offset:27648
	ds_read_b64_tr_b16 v[110:111], v187 offset:28160
	s_waitcnt lgkmcnt(14)
	v_mfma_f32_32x32x16_f16 v[80:95], v[148:151], v[112:115], v[80:95]
	v_pk_add_f16 v49, v100, v49
	v_cvt_pk_f16_f32 v128, v56, v57
	v_cvt_pk_f16_f32 v129, v58, v59
	v_pk_add_f16 v50, v134, v135
	ds_read_b64_tr_b16 v[100:101], v187 offset:31744
	ds_read_b64_tr_b16 v[102:103], v187 offset:32256
	v_mfma_f32_32x32x16_f16 v[32:47], v[144:147], v[112:115], v[32:47]
	v_pk_add_f16 v116, v128, v129
	v_pk_add_f16 v48, v48, v50
	v_cvt_pk_f16_f32 v130, v60, v61
	v_cvt_pk_f16_f32 v131, v62, v63
	s_and_b64 vcc, exec, s[2:3]
	v_pk_add_f16 v112, v49, v48
	v_pk_add_f16 v113, v130, v131
	s_cbranch_vccnz .LBB2_27
	v_pk_add_f16 v48, v116, v113
	v_max3_f32 v50, v80, v81, v32
	v_max3_f32 v51, v82, v83, v33
	s_mov_b32 s2, 0x41000000
	v_pk_add_f16 v48, v112, v48
	s_mov_b64 s[8:9], 0
	v_cvt_f32_f16_e32 v49, v48
	v_cvt_f32_f16_sdwa v48, v48 dst_sel:DWORD dst_unused:UNUSED_PAD src0_sel:WORD_1
	v_add_f32_e32 v48, v48, v49
	v_add_f32_e32 v188, v188, v48
	v_max3_f32 v48, v50, v34, v35
	v_max3_f32 v49, v51, v86, v87
	s_nop 0
	v_max3_f32 v48, v48, v84, v85
	v_max3_f32 v49, v49, v38, v39
	s_nop 0
	v_max3_f32 v48, v48, v36, v37
	v_max3_f32 v49, v49, v90, v91
	s_nop 0
	v_max3_f32 v48, v48, v88, v89
	v_max3_f32 v49, v49, v42, v43
	s_nop 0
	v_max3_f32 v48, v48, v40, v41
	v_max3_f32 v49, v49, v94, v95
	s_nop 0
	v_max3_f32 v48, v48, v92, v93
	v_max3_f32 v49, v49, v46, v47
	s_nop 0
	v_max3_f32 v48, v48, v44, v45
	s_nop 0
	v_max_f32 v48, v48, v49
	s_nop 0
	v_mov_b32_e32 v49, v48
	s_nop 1
	v_permlane32_swap_b32_e32 v48, v49
	v_max_f32 v48, v48, v49
	s_nop 0
	v_cmp_lt_f32_e32 vcc, s2, v48
	s_cbranch_vccnz .LBB2_34
